# static priority raise for the output-wave half moved to the prologue (right after the first codebook wait), instead of only from the main loop on
# speedup vs baseline: 1.0018x; 1.0018x over previous
.LBB0_5:
	s_or_b64 exec, exec, s[4:5]
	s_lshr_b32 s33, s3, 6
	s_lshl_b32 s3, s33, 7
	v_bfe_u32 v70, v0, 4, 2
	s_lshl_b32 s4, s2, 2
	v_or_b32_e32 v18, s3, v70
	v_lshlrev_b32_e32 v2, 4, v0
	s_and_b32 s25, s4, 28
	v_and_b32_e32 v84, 0xf0, v2
	v_or_b32_e32 v2, s25, v18
	s_add_i32 s5, s4, 4
	v_lshl_or_b32 v2, v2, 8, v84
	s_and_b32 s34, s5, 28
	s_waitcnt lgkmcnt(0)
	global_load_dwordx4 v[2:5], v2, s[22:23]
	v_or_b32_e32 v6, s34, v18
	s_add_i32 s5, s4, 8
	v_lshl_or_b32 v6, v6, 8, v84
	s_and_b32 s35, s5, 28
	global_load_dwordx4 v[6:9], v6, s[22:23]
	v_or_b32_e32 v10, s35, v18
	s_add_i32 s5, s4, 12
	v_lshl_or_b32 v10, v10, 8, v84
	s_and_b32 s36, s5, 28
	global_load_dwordx4 v[10:13], v10, s[22:23]
	v_or_b32_e32 v14, s36, v18
	v_lshl_or_b32 v14, v14, 8, v84
	s_xor_b32 s37, s25, 16
	global_load_dwordx4 v[14:17], v14, s[22:23]
	v_or_b32_e32 v19, s37, v18
	s_add_i32 s5, s4, 20
	v_lshl_or_b32 v19, v19, 8, v84
	s_and_b32 s38, s5, 28
	global_load_dwordx4 v[46:49], v19, s[22:23]
	v_or_b32_e32 v20, s38, v18
	s_add_i32 s7, s4, 24
	v_lshl_or_b32 v20, v20, 8, v84
	s_and_b32 s39, s7, 28
	global_load_dwordx4 v[50:53], v20, s[22:23]
	v_or_b32_e32 v20, s39, v18
	s_add_i32 s4, s4, 28
	v_lshl_or_b32 v20, v20, 8, v84
	s_and_b32 s40, s4, 28
	global_load_dwordx4 v[58:61], v20, s[22:23]
	v_or_b32_e32 v18, s40, v18
	v_lshl_or_b32 v18, v18, 8, v84
	global_load_dwordx4 v[62:65], v18, s[22:23]
	v_lshlrev_b32_e32 v19, 3, v0
	s_mul_i32 s6, s33, 0x1200
	v_and_b32_e32 v19, 0x78, v19
	v_or_b32_e32 v85, 32, v70
	v_or_b32_e32 v93, s6, v19
	v_or_b32_e32 v19, s3, v85
	v_bfe_u32 v184, v0, 5, 1
	v_and_b32_e32 v181, 31, v0
	s_movk_i32 s5, 0x90
	v_mov_b32_e32 v18, s6
	v_or_b32_e32 v20, s25, v19
	v_lshlrev_b32_e32 v182, 4, v184
	v_mad_u32_u24 v18, v181, s5, v18
	v_or_b32_e32 v21, s34, v19
	v_or_b32_e32 v22, s35, v19
	v_or_b32_e32 v23, s36, v19
	v_or_b32_e32 v24, s37, v19
	v_or_b32_e32 v25, s38, v19
	v_or_b32_e32 v26, s39, v19
	v_or_b32_e32 v19, s40, v19
	v_lshl_or_b32 v43, v20, 8, v84
	v_add_u32_e32 v82, v18, v182
	v_lshl_or_b32 v44, v21, 8, v84
	v_lshl_or_b32 v45, v22, 8, v84
	v_lshl_or_b32 v71, v23, 8, v84
	v_lshl_or_b32 v72, v24, 8, v84
	v_lshl_or_b32 v73, v25, 8, v84
	v_lshl_or_b32 v74, v26, 8, v84
	v_lshl_or_b32 v75, v19, 8, v84
	global_load_dwordx4 v[66:69], v43, s[22:23]
	global_load_dwordx4 v[54:57], v44, s[22:23]
	global_load_dwordx4 v[38:41], v45, s[22:23]
	global_load_dwordx4 v[34:37], v71, s[22:23]
	global_load_dwordx4 v[30:33], v72, s[22:23]
	global_load_dwordx4 v[26:29], v73, s[22:23]
	global_load_dwordx4 v[22:25], v74, s[22:23]
	global_load_dwordx4 v[18:21], v75, s[22:23]
	v_or_b32_e32 v42, s25, v70
	v_or_b32_e32 v43, s34, v70
	v_or_b32_e32 v44, s35, v70
	v_or_b32_e32 v45, s36, v70
	s_waitcnt vmcnt(15)
	s_cmp_lt_u32 s33, 4
	s_cbranch_scc1 .Lno_stagger
	s_sleep 10
	s_branch .Lpro_go
.Lno_stagger:
	s_setprio 2
